# A/B of the static priority raise: waves 0-3 instead of waves 4-7 (same phases)
# speedup vs baseline: 1.0006x; 1.0006x over previous
.LBB0_463:
	s_andn2_b64 vcc, exec, s[0:1]
	s_cbranch_vccnz .LBB0_748
	v_writelane_b32 v255, s86, 39
	s_movk_i32 s1, 0x800
	s_cmpk_gt_i32 s20, 0xff
	v_writelane_b32 v255, s87, 40
	v_writelane_b32 v255, s82, 43
	v_writelane_b32 v255, s94, 44
	s_cbranch_scc1 .LBB0_493
	s_add_u32 s78, s76, 0x46600000
	s_addc_u32 s79, s77, 0
	s_add_u32 s80, s76, 0x15e00000
	s_addc_u32 s81, s77, 0
	s_lshl_b32 s82, s71, 3
	s_or_b32 s84, s82, 1
	s_sub_i32 s83, 0xff, s82
	s_sub_i32 s85, 0xff, s84
	s_lshl_b32 s86, s71, 8
	s_cmp_gt_i32 s71, 0
	s_waitcnt lgkmcnt(0)
	s_cselect_b64 s[42:43], -1, 0
	s_cmp_gt_i32 s71, 1
	s_cselect_b64 s[44:45], -1, 0
	s_cmp_gt_i32 s71, 2
	s_waitcnt vmcnt(0)
	v_ashrrev_i32_e32 v17, 3, v126
	s_cselect_b64 s[46:47], -1, 0
	s_cmp_gt_i32 s71, 3
	v_and_b32_e32 v86, 0x7f, v126
	v_and_b32_e32 v87, -16, v17
	v_lshl_add_u32 v91, v127, 2, 0
	v_lshlrev_b32_e32 v3, 1, v127
	s_cselect_b64 s[48:49], -1, 0
	s_cmp_gt_i32 s71, 4
	v_and_b32_e32 v1, 15, v126
	v_lshrrev_b32_e32 v2, 4, v127
	v_sub_u32_e32 v92, v91, v3
	v_mul_u32_u24_e32 v3, 0x90, v86
	v_lshlrev_b32_e32 v4, 1, v87
	s_cselect_b64 s[50:51], -1, 0
	s_cmp_gt_i32 s71, 5
	s_movk_i32 s0, 0x8e
	v_add3_u32 v94, 0, v3, v4
	v_lshlrev_b32_e32 v4, 3, v2
	v_lshlrev_b32_e32 v2, 2, v2
	v_lshlrev_b32_e32 v6, 4, v126
	v_mul_u32_u24_e32 v100, 0x90, v1
	s_cselect_b64 s[52:53], -1, 0
	s_cmp_gt_i32 s71, 6
	v_mad_u32_u24 v93, v127, s0, v92
	v_sub_u32_e32 v2, v1, v2
	v_and_b32_e32 v76, 0x70, v6
	s_movk_i32 s0, 0x110
	v_add3_u32 v101, 0, v100, v4
	s_cselect_b64 s[54:55], -1, 0
	s_cmp_gt_i32 s71, 7
	v_and_b32_e32 v5, 48, v127
	v_mul_lo_u32 v6, v17, s0
	v_lshlrev_b32_e32 v7, 1, v76
	v_cmp_gt_i32_e32 vcc, 0, v2
	v_cmp_gt_i32_e64 s[58:59], 1, v2
	v_cmp_gt_i32_e64 s[62:63], 2, v2
	v_cmp_gt_i32_e64 s[40:41], 3, v2
	v_lshlrev_b32_e32 v2, 7, v1
	v_add_u32_e32 v103, 0x1200, v101
	s_movk_i32 s0, 0x1000
	s_cselect_b64 s[56:57], -1, 0
	s_lshl_b32 s87, s71, 4
	v_add_u32_e32 v95, 0, v5
	v_add3_u32 v96, 0, v6, v7
	v_mul_u32_u24_e32 v6, 0x48, v1
	v_add_u32_e32 v102, 0x900, v101
	v_add3_u32 v8, v103, v2, s0
	v_add_u32_e32 v104, 0x1b00, v101
	s_movk_i32 s0, 0x1800
	s_cmp_lt_u32 s16, 64
	v_lshl_add_u32 v97, v6, 1, v95
	v_add_u32_e32 v6, v101, v2
	v_add3_u32 v7, v102, v2, s1
	v_add3_u32 v2, v104, v2, s0
	s_cselect_b64 s[18:19], -1, 0
	v_or_b32_e32 v1, s87, v1
	s_movk_i32 s0, 0x90
	s_and_b64 s[62:63], s[40:41], s[62:63]
	v_or_b32_e32 v89, 1, v87
	v_mul_i32_i24_e32 v3, 0xffffff74, v127
	v_and_b32_e32 v5, 48, v126
	v_mul_lo_u32 v105, v1, s0
	s_lshl_b32 s0, s71, 5
	s_and_b64 s[72:73], s[62:63], s[58:59]
	v_sub_u32_e32 v88, 0xff, v87
	v_sub_u32_e32 v90, 0xff, v89
	v_mov_b32_e32 v77, v34
	v_add_u32_e32 v98, 0x1200, v97
	v_add_u32_e32 v99, 0x1b00, v97
	v_add3_u32 v106, 0, v105, v4
	v_sub_u32_e32 v107, 0, v17
	v_lshrrev_b32_e32 v218, 4, v127
	v_lshl_add_u32 v218, v218, 2, s87
	s_sub_i32 s16, 0, s82
	v_sub_u32_e32 v108, 0, v87
	v_add_u32_e32 v109, v93, v3
	v_add_u32_e32 v110, s0, v6
	v_add_u32_e32 v111, s0, v7
	v_add_u32_e32 v112, s0, v8
	v_add_u32_e32 v113, s0, v2
	v_add_u32_e32 v114, 0, v5
	s_and_b64 s[2:3], s[72:73], vcc
	s_mov_b32 s17, s20
	s_cmp_lt_u32 s71, 4
	s_cbranch_scc0 .Lprio_gla
	s_setprio 1

.LBB0_801:
	s_andn2_b64 vcc, exec, s[0:1]
	s_cbranch_vccnz .LBB0_874
	s_mov_b32 s0, 0
	s_add_i32 s28, s0, s84
	s_waitcnt vmcnt(0)
	v_add_u32_e32 v2, s0, v0
	s_cmpk_gt_i32 s28, 0x23f
	v_readfirstlane_b32 s1, v2
	s_cbranch_scc1 .LBB0_823
	s_ashr_i32 s36, s1, 6
	s_ashr_i32 s1, s0, 31
	v_readlane_b32 s2, v254, 2
	v_readlane_b32 s3, v254, 3
	s_add_u32 s2, s2, s0
	s_addc_u32 s3, s3, s1
	s_add_u32 s14, s2, 0x32600000
	s_addc_u32 s15, s3, 0
	s_lshr_b64 s[16:17], s[24:25], 1
	s_lshr_b32 s17, s25, 1
	s_mul_i32 s17, s17, 0x480000
	s_mul_hi_u32 s18, s16, 0x480000
	s_mul_i32 s45, s16, 0x480000
	s_lshl_b32 s16, s36, 8
	s_add_i32 s20, s18, s17
	s_lshl_b32 s37, s82, 9
	s_lshl_b32 s46, s36, 10
	s_not_b32 s47, s16
	s_lshl_b64 s[18:19], s[0:1], 3
	s_waitcnt lgkmcnt(0)
	v_readlane_b32 s42, v254, 4
	v_readlane_b32 s43, v254, 5
	s_add_u32 s18, s42, s18
	v_bfe_u32 v1, v2, 5, 1
	s_addc_u32 s19, s43, s19
	v_and_b32_e32 v165, 31, v2
	v_lshlrev_b32_e32 v218, 3, v1
	v_mov_b32_e32 v219, v34
	v_lshlrev_b32_e32 v4, 4, v1
	v_mov_b32_e32 v5, v34
	s_movk_i32 s17, 0x200
	s_load_dwordx2 s[42:43], s[18:19], 0xc8
	s_mul_i32 s18, s36, 0x4200
	v_mul_u32_u24_e32 v3, 0x140, v165
	v_lshl_add_u64 v[220:221], s[14:15], 0, v[4:5]
	v_cmp_gt_i32_e64 s[40:41], s17, v2
	s_add_i32 s17, s18, 0
	v_lshl_add_u64 v[222:223], s[14:15], 0, v[218:219]
	v_lshl_add_u64 v[6:7], s[2:3], 0, v[218:219]
	s_mov_b64 s[14:15], 0x41600000
	v_or_b32_e32 v214, 0x2110000, v3
	v_mov_b32_e32 v3, s17
	s_ashr_i32 s17, s16, 31
	v_lshl_add_u64 v[224:225], v[6:7], 0, s[14:15]
	v_readlane_b32 s14, v255, 9
	v_add_u32_e32 v167, s0, v217
	s_add_u32 s14, s14, s0
	v_readlane_b32 s0, v255, 10
	s_movk_i32 s19, 0x210
	s_addc_u32 s15, s0, s1
	v_mad_u32_u24 v8, v165, s19, v3
	v_ashrrev_i32_e32 v3, 31, v2
	s_add_u32 s0, s14, s45
	v_lshl_add_u32 v219, v2, 4, 0
	v_lshlrev_b64 v[2:3], 4, v[2:3]
	s_addc_u32 s1, s15, s20
	v_lshl_add_u64 v[226:227], s[0:1], 0, v[2:3]
	s_lshl_b32 s0, s28, 3
	s_ashr_i32 s29, s28, 31
	s_add_i32 s44, s0, 0xfffff000
	s_lshl_b64 s[0:1], s[28:29], 13
	s_add_u32 s0, s45, s0
	s_addc_u32 s1, s20, s1
	s_add_u32 s0, s14, s0
	s_addc_u32 s1, s15, s1
	v_lshlrev_b32_e32 v4, 4, v165
	v_lshl_add_u64 v[228:229], s[0:1], 0, v[2:3]
	s_movk_i32 s0, 0x1080
	v_mad_u64_u32 v[2:3], s[0:1], v1, s0, v[4:5]
	s_lshl_b64 s[0:1], s[16:17], 1
	s_add_u32 s0, s2, s0
	s_addc_u32 s1, s3, s1
	v_lshl_add_u64 v[230:231], s[0:1], 0, v[2:3]
	v_mov_b32_e32 v2, s18
	v_mad_u32_u24 v1, v1, s19, v2
	v_mov_b32_e32 v215, v34
	v_mul_u32_u24_e32 v216, 0x840, v165
	v_add3_u32 v246, v1, v4, 0
	v_add_u32_e32 v247, v8, v218
	s_cmp_lt_u32 s36, 4
	s_cbranch_scc0 .Lprio_hyc
	s_setprio 1
